# mlstm_local: K-step loop fully unrolled with the next step's eight operand loads issued one step ahead into alternate registers (base addresses computed once, first loads before accumulator zeroing)
# baseline (speedup 1.0000x reference)
.LBB0_659:
	s_or_b64 exec, exec, s[30:31]
	v_mad_i32_i24 v2, v0, 6, v2
	v_ashrrev_i32_e32 v3, 31, v2
	v_ashrrev_i32_e32 v5, 31, v4
	v_lshlrev_b64 v[2:3], 19, v[2:3]
	v_lshlrev_b64 v[4:5], 8, v[4:5]
	v_lshl_add_u64 v[2:3], v[2:3], 0, v[4:5]
	v_lshl_add_u64 v[118:119], v[112:113], 0, v[2:3]
	s_mov_b32 s33, 0x3b044000
	v_add_co_u32_e32 v188, vcc, s33, v118
	s_nop 1
	v_addc_co_u32_e32 v189, vcc, 0, v119, vcc
	s_mov_b32 s33, 0x3b064000
	v_add_co_u32_e32 v190, vcc, s33, v118
	s_nop 1
	v_addc_co_u32_e32 v191, vcc, 0, v119, vcc
	s_mov_b32 s33, 0x3a444000
	v_add_co_u32_e32 v196, vcc, s33, v118
	s_nop 1
	v_addc_co_u32_e32 v197, vcc, 0, v119, vcc
	s_mov_b32 s33, 0x3a464000
	v_add_co_u32_e32 v198, vcc, s33, v118
	s_nop 1
	v_addc_co_u32_e32 v199, vcc, 0, v119, vcc
	s_mov_b32 s33, 0x3b084000
	v_add_co_u32_e32 v192, vcc, s33, v118
	s_nop 1
	v_addc_co_u32_e32 v193, vcc, 0, v119, vcc
	s_mov_b32 s33, 0x3b0a4000
	v_add_co_u32_e32 v194, vcc, s33, v118
	s_nop 1
	v_addc_co_u32_e32 v195, vcc, 0, v119, vcc
	s_mov_b32 s33, 0x3a484000
	v_add_co_u32_e32 v200, vcc, s33, v118
	s_nop 1
	v_addc_co_u32_e32 v201, vcc, 0, v119, vcc
	s_mov_b32 s33, 0x3a4a4000
	v_add_co_u32_e32 v202, vcc, s33, v118
	s_nop 1
	v_addc_co_u32_e32 v203, vcc, 0, v119, vcc
	global_load_dwordx4 v[82:85], v[188:189], off offset:2048
	global_load_dwordx4 v[78:81], v[190:191], off offset:2048
	global_load_dwordx4 v[86:89], v[196:197], off offset:2048
	global_load_dwordx4 v[90:93], v[198:199], off offset:2048
	global_load_dwordx4 v[70:73], v[192:193], off offset:2048
	global_load_dwordx4 v[74:77], v[194:195], off offset:2048
	global_load_dwordx4 v[152:155], v[200:201], off offset:2048
	global_load_dwordx4 v[156:159], v[202:203], off offset:2048
	v_mov_b32_e32 v2, 0
	s_mov_b64 s[30:31], 0
	v_mov_b32_e32 v0, v126
	v_mov_b32_e32 v3, v2
	v_mov_b32_e32 v4, v2
	v_mov_b32_e32 v5, v2
	v_mov_b32_e32 v18, v2
	v_mov_b32_e32 v19, v2
	v_mov_b32_e32 v20, v2
	v_mov_b32_e32 v21, v2
	v_mov_b32_e32 v38, v2
	v_mov_b32_e32 v39, v2
	v_mov_b32_e32 v40, v2
	v_mov_b32_e32 v41, v2
	v_mov_b32_e32 v54, v2
	v_mov_b32_e32 v55, v2
	v_mov_b32_e32 v56, v2
	v_mov_b32_e32 v57, v2
	v_mov_b32_e32 v10, v2
	v_mov_b32_e32 v11, v2
	v_mov_b32_e32 v12, v2
	v_mov_b32_e32 v13, v2
	v_mov_b32_e32 v30, v2
	v_mov_b32_e32 v31, v2
	v_mov_b32_e32 v32, v2
	v_mov_b32_e32 v33, v2
	v_mov_b32_e32 v50, v2
	v_mov_b32_e32 v51, v2
	v_mov_b32_e32 v52, v2
	v_mov_b32_e32 v53, v2
	v_mov_b32_e32 v66, v2
	v_mov_b32_e32 v67, v2
	v_mov_b32_e32 v68, v2
	v_mov_b32_e32 v69, v2
	v_mov_b32_e32 v62, v2
	v_mov_b32_e32 v63, v2
	v_mov_b32_e32 v64, v2
	v_mov_b32_e32 v65, v2
	v_mov_b32_e32 v46, v2
	v_mov_b32_e32 v47, v2
	v_mov_b32_e32 v48, v2
	v_mov_b32_e32 v49, v2
	v_mov_b32_e32 v26, v2
	v_mov_b32_e32 v27, v2
	v_mov_b32_e32 v28, v2
	v_mov_b32_e32 v29, v2
	v_mov_b32_e32 v14, v2
	v_mov_b32_e32 v15, v2
	v_mov_b32_e32 v16, v2
	v_mov_b32_e32 v17, v2
	v_mov_b32_e32 v58, v2
	v_mov_b32_e32 v59, v2
	v_mov_b32_e32 v60, v2
	v_mov_b32_e32 v61, v2
	v_mov_b32_e32 v42, v2
	v_mov_b32_e32 v43, v2
	v_mov_b32_e32 v44, v2
	v_mov_b32_e32 v45, v2
	v_mov_b32_e32 v22, v2
	v_mov_b32_e32 v23, v2
	v_mov_b32_e32 v24, v2
	v_mov_b32_e32 v25, v2
	v_mov_b32_e32 v6, v2
	v_mov_b32_e32 v7, v2
	v_mov_b32_e32 v8, v2
	v_mov_b32_e32 v9, v2
	v_mov_b32_e32 v116, v2
	v_mov_b32_e32 v117, v2
	v_mov_b32_e32 v114, v2
	v_mov_b32_e32 v115, v2
.LBB0_660:
	global_load_dwordx4 v[172:175], v[188:189], off offset:2112
	global_load_dwordx4 v[168:171], v[190:191], off offset:2112
	global_load_dwordx4 v[176:179], v[196:197], off offset:2112
	global_load_dwordx4 v[180:183], v[198:199], off offset:2112
	global_load_dwordx4 v[160:163], v[192:193], off offset:2112
	global_load_dwordx4 v[164:167], v[194:195], off offset:2112
	global_load_dwordx4 v[224:227], v[200:201], off offset:2112
	global_load_dwordx4 v[228:231], v[202:203], off offset:2112
	s_waitcnt vmcnt(8)
	ds_read_b128 v[98:101], v0
	ds_read_b128 v[94:97], v0 offset:16
	v_lshlrev_b32_e32 v102, 16, v86
	v_lshlrev_b32_e32 v136, 16, v87
	v_and_b32_e32 v104, 0xffff0000, v86
	v_and_b32_e32 v103, 0xffff0000, v90
	v_and_b32_e32 v137, 0xffff0000, v91
	s_waitcnt lgkmcnt(1)
	v_pk_mul_f32 v[102:103], v[98:99], v[102:103]
	v_lshlrev_b32_e32 v105, 16, v90
	v_pk_mul_f32 v[136:137], v[100:101], v[136:137]
	v_and_b32_e32 v86, 0xffff0000, v87
	v_lshlrev_b32_e32 v87, 16, v91
	v_lshlrev_b32_e32 v138, 16, v88
	v_and_b32_e32 v139, 0xffff0000, v92
	v_pk_mul_f32 v[134:135], v[98:99], v[104:105] op_sel:[1,0] op_sel_hi:[0,1]
	v_pk_mul_f32 v[90:91], v[100:101], v[86:87] op_sel:[1,0] op_sel_hi:[0,1]
	s_waitcnt lgkmcnt(0)
	v_pk_mul_f32 v[138:139], v[94:95], v[138:139]
	v_and_b32_e32 v140, 0xffff0000, v88
	v_lshlrev_b32_e32 v141, 16, v92
	v_lshlrev_b32_e32 v144, 16, v89
	v_and_b32_e32 v145, 0xffff0000, v93
	v_pk_fma_f32 v[104:105], v[98:99], v[104:105], v[102:103] op_sel:[1,0,0] op_sel_hi:[0,1,1]
	v_pk_fma_f32 v[86:87], v[100:101], v[86:87], v[136:137] op_sel:[1,0,0] op_sel_hi:[0,1,1]
	v_pk_mul_f32 v[144:145], v[96:97], v[144:145]
	v_and_b32_e32 v88, 0xffff0000, v89
	v_lshlrev_b32_e32 v89, 16, v93
	v_pk_add_f32 v[86:87], v[104:105], v[86:87]
	v_pk_fma_f32 v[104:105], v[94:95], v[140:141], v[138:139] op_sel:[1,0,0] op_sel_hi:[0,1,1]
	v_pk_mul_f32 v[92:93], v[96:97], v[88:89] op_sel:[1,0] op_sel_hi:[0,1]
	v_pk_add_f32 v[86:87], v[104:105], v[86:87]
	v_pk_fma_f32 v[88:89], v[96:97], v[88:89], v[144:145] op_sel:[1,0,0] op_sel_hi:[0,1,1]
	v_pk_add_f32 v[104:105], v[88:89], v[86:87]
	v_cvt_pk_bf16_f32 v86, v102, v134
	v_cvt_pk_bf16_f32 v87, v136, v90
	v_cvt_pk_bf16_f32 v90, v135, v103
	v_pk_add_f32 v[116:117], v[116:117], v[104:105]
	v_cvt_pk_bf16_f32 v91, v91, v137
	v_pk_mul_f32 v[142:143], v[94:95], v[140:141] op_sel:[1,0] op_sel_hi:[0,1]
	v_cvt_pk_bf16_f32 v88, v138, v142
	v_cvt_pk_bf16_f32 v89, v144, v92
	v_cvt_pk_bf16_f32 v92, v143, v139
	v_cvt_pk_bf16_f32 v93, v93, v145
	v_mfma_f32_16x16x32_bf16 v[66:69], v[82:85], v[86:89], v[66:69]
	v_lshlrev_b32_e32 v120, 16, v152
	v_lshlrev_b32_e32 v142, 16, v153
	v_and_b32_e32 v121, 0xffff0000, v156
	v_and_b32_e32 v143, 0xffff0000, v157
	v_pk_mul_f32 v[120:121], v[98:99], v[120:121]
	v_and_b32_e32 v138, 0xffff0000, v152
	v_lshlrev_b32_e32 v139, 16, v156
	v_pk_mul_f32 v[142:143], v[100:101], v[142:143]
	v_and_b32_e32 v102, 0xffff0000, v153
	v_lshlrev_b32_e32 v103, 16, v157
	v_lshlrev_b32_e32 v144, 16, v154
	v_and_b32_e32 v145, 0xffff0000, v158
	v_pk_mul_f32 v[140:141], v[98:99], v[138:139] op_sel:[1,0] op_sel_hi:[0,1]
	v_pk_mul_f32 v[134:135], v[100:101], v[102:103] op_sel:[1,0] op_sel_hi:[0,1]
	v_pk_mul_f32 v[144:145], v[94:95], v[144:145]
	v_and_b32_e32 v146, 0xffff0000, v154
	v_lshlrev_b32_e32 v147, 16, v158
	v_lshlrev_b32_e32 v150, 16, v155
	v_and_b32_e32 v151, 0xffff0000, v159
	v_pk_fma_f32 v[98:99], v[98:99], v[138:139], v[120:121] op_sel:[1,0,0] op_sel_hi:[0,1,1]
	v_pk_fma_f32 v[100:101], v[100:101], v[102:103], v[142:143] op_sel:[1,0,0] op_sel_hi:[0,1,1]
	v_pk_mul_f32 v[148:149], v[94:95], v[146:147] op_sel:[1,0] op_sel_hi:[0,1]
	v_pk_mul_f32 v[150:151], v[96:97], v[150:151]
	v_and_b32_e32 v104, 0xffff0000, v155
	v_lshlrev_b32_e32 v105, 16, v159
	v_pk_add_f32 v[98:99], v[98:99], v[100:101]
	v_pk_fma_f32 v[94:95], v[94:95], v[146:147], v[144:145] op_sel:[1,0,0] op_sel_hi:[0,1,1]
	v_pk_mul_f32 v[136:137], v[96:97], v[104:105] op_sel:[1,0] op_sel_hi:[0,1]
	v_pk_add_f32 v[94:95], v[94:95], v[98:99]
	v_pk_fma_f32 v[96:97], v[96:97], v[104:105], v[150:151] op_sel:[1,0,0] op_sel_hi:[0,1,1]
	v_pk_add_f32 v[98:99], v[96:97], v[94:95]
	v_cvt_pk_bf16_f32 v94, v120, v140
	v_cvt_pk_bf16_f32 v95, v142, v134
	v_cvt_pk_bf16_f32 v96, v144, v148
	v_cvt_pk_bf16_f32 v97, v150, v136
	v_pk_add_f32 v[114:115], v[114:115], v[98:99]
	v_cvt_pk_bf16_f32 v98, v141, v121
	v_cvt_pk_bf16_f32 v99, v135, v143
	v_cvt_pk_bf16_f32 v100, v149, v145
	v_cvt_pk_bf16_f32 v101, v137, v151
	v_mfma_f32_16x16x32_bf16 v[50:53], v[82:85], v[90:93], v[50:53]
	v_mfma_f32_16x16x32_bf16 v[30:33], v[82:85], v[94:97], v[30:33]
	v_mfma_f32_16x16x32_bf16 v[10:13], v[82:85], v[98:101], v[10:13]
	v_mfma_f32_16x16x32_bf16 v[54:57], v[78:81], v[86:89], v[54:57]
	v_mfma_f32_16x16x32_bf16 v[38:41], v[78:81], v[90:93], v[38:41]
	v_mfma_f32_16x16x32_bf16 v[18:21], v[78:81], v[94:97], v[18:21]
	v_mfma_f32_16x16x32_bf16 v[2:5], v[78:81], v[98:101], v[2:5]
	v_mfma_f32_16x16x32_bf16 v[62:65], v[70:73], v[86:89], v[62:65]
	v_mfma_f32_16x16x32_bf16 v[46:49], v[70:73], v[90:93], v[46:49]
	v_mfma_f32_16x16x32_bf16 v[26:29], v[70:73], v[94:97], v[26:29]
	v_mfma_f32_16x16x32_bf16 v[14:17], v[70:73], v[98:101], v[14:17]
	v_mfma_f32_16x16x32_bf16 v[58:61], v[74:77], v[86:89], v[58:61]
	v_mfma_f32_16x16x32_bf16 v[42:45], v[74:77], v[90:93], v[42:45]
	v_mfma_f32_16x16x32_bf16 v[22:25], v[74:77], v[94:97], v[22:25]
	v_mfma_f32_16x16x32_bf16 v[6:9], v[74:77], v[98:101], v[6:9]
	global_load_dwordx4 v[82:85], v[188:189], off offset:2176
	global_load_dwordx4 v[78:81], v[190:191], off offset:2176
	global_load_dwordx4 v[86:89], v[196:197], off offset:2176
	global_load_dwordx4 v[90:93], v[198:199], off offset:2176
	global_load_dwordx4 v[70:73], v[192:193], off offset:2176
	global_load_dwordx4 v[74:77], v[194:195], off offset:2176
	global_load_dwordx4 v[152:155], v[200:201], off offset:2176
	global_load_dwordx4 v[156:159], v[202:203], off offset:2176
	s_waitcnt vmcnt(8)
	ds_read_b128 v[98:101], v0 offset:128
	ds_read_b128 v[94:97], v0 offset:144
	v_lshlrev_b32_e32 v102, 16, v176
	v_lshlrev_b32_e32 v136, 16, v177
	v_and_b32_e32 v104, 0xffff0000, v176
	v_and_b32_e32 v103, 0xffff0000, v180
	v_and_b32_e32 v137, 0xffff0000, v181
	s_waitcnt lgkmcnt(1)
	v_pk_mul_f32 v[102:103], v[98:99], v[102:103]
	v_lshlrev_b32_e32 v105, 16, v180
	v_pk_mul_f32 v[136:137], v[100:101], v[136:137]
	v_and_b32_e32 v176, 0xffff0000, v177
	v_lshlrev_b32_e32 v177, 16, v181
	v_lshlrev_b32_e32 v138, 16, v178
	v_and_b32_e32 v139, 0xffff0000, v182
	v_pk_mul_f32 v[134:135], v[98:99], v[104:105] op_sel:[1,0] op_sel_hi:[0,1]
	v_pk_mul_f32 v[180:181], v[100:101], v[176:177] op_sel:[1,0] op_sel_hi:[0,1]
	s_waitcnt lgkmcnt(0)
	v_pk_mul_f32 v[138:139], v[94:95], v[138:139]
	v_and_b32_e32 v140, 0xffff0000, v178
	v_lshlrev_b32_e32 v141, 16, v182
	v_lshlrev_b32_e32 v144, 16, v179
	v_and_b32_e32 v145, 0xffff0000, v183
	v_pk_fma_f32 v[104:105], v[98:99], v[104:105], v[102:103] op_sel:[1,0,0] op_sel_hi:[0,1,1]
	v_pk_fma_f32 v[176:177], v[100:101], v[176:177], v[136:137] op_sel:[1,0,0] op_sel_hi:[0,1,1]
	v_pk_mul_f32 v[144:145], v[96:97], v[144:145]
	v_and_b32_e32 v178, 0xffff0000, v179
	v_lshlrev_b32_e32 v179, 16, v183
	v_pk_add_f32 v[176:177], v[104:105], v[176:177]
	v_pk_fma_f32 v[104:105], v[94:95], v[140:141], v[138:139] op_sel:[1,0,0] op_sel_hi:[0,1,1]
	v_pk_mul_f32 v[182:183], v[96:97], v[178:179] op_sel:[1,0] op_sel_hi:[0,1]
	v_pk_add_f32 v[176:177], v[104:105], v[176:177]
	v_pk_fma_f32 v[178:179], v[96:97], v[178:179], v[144:145] op_sel:[1,0,0] op_sel_hi:[0,1,1]
	v_pk_add_f32 v[104:105], v[178:179], v[176:177]
	v_cvt_pk_bf16_f32 v176, v102, v134
	v_cvt_pk_bf16_f32 v177, v136, v180
	v_cvt_pk_bf16_f32 v180, v135, v103
	v_pk_add_f32 v[116:117], v[116:117], v[104:105]
	v_cvt_pk_bf16_f32 v181, v181, v137
	v_pk_mul_f32 v[142:143], v[94:95], v[140:141] op_sel:[1,0] op_sel_hi:[0,1]
	v_cvt_pk_bf16_f32 v178, v138, v142
	v_cvt_pk_bf16_f32 v179, v144, v182
	v_cvt_pk_bf16_f32 v182, v143, v139
	v_cvt_pk_bf16_f32 v183, v183, v145
	v_mfma_f32_16x16x32_bf16 v[66:69], v[172:175], v[176:179], v[66:69]
	v_lshlrev_b32_e32 v120, 16, v224
	v_lshlrev_b32_e32 v142, 16, v225
	v_and_b32_e32 v121, 0xffff0000, v228
	v_and_b32_e32 v143, 0xffff0000, v229
	v_pk_mul_f32 v[120:121], v[98:99], v[120:121]
	v_and_b32_e32 v138, 0xffff0000, v224
	v_lshlrev_b32_e32 v139, 16, v228
	v_pk_mul_f32 v[142:143], v[100:101], v[142:143]
	v_and_b32_e32 v102, 0xffff0000, v225
	v_lshlrev_b32_e32 v103, 16, v229
	v_lshlrev_b32_e32 v144, 16, v226
	v_and_b32_e32 v145, 0xffff0000, v230
	v_pk_mul_f32 v[140:141], v[98:99], v[138:139] op_sel:[1,0] op_sel_hi:[0,1]
	v_pk_mul_f32 v[134:135], v[100:101], v[102:103] op_sel:[1,0] op_sel_hi:[0,1]
	v_pk_mul_f32 v[144:145], v[94:95], v[144:145]
	v_and_b32_e32 v146, 0xffff0000, v226
	v_lshlrev_b32_e32 v147, 16, v230
	v_lshlrev_b32_e32 v150, 16, v227
	v_and_b32_e32 v151, 0xffff0000, v231
	v_pk_fma_f32 v[98:99], v[98:99], v[138:139], v[120:121] op_sel:[1,0,0] op_sel_hi:[0,1,1]
	v_pk_fma_f32 v[100:101], v[100:101], v[102:103], v[142:143] op_sel:[1,0,0] op_sel_hi:[0,1,1]
	v_pk_mul_f32 v[148:149], v[94:95], v[146:147] op_sel:[1,0] op_sel_hi:[0,1]
	v_pk_mul_f32 v[150:151], v[96:97], v[150:151]
	v_and_b32_e32 v104, 0xffff0000, v227
	v_lshlrev_b32_e32 v105, 16, v231
	v_pk_add_f32 v[98:99], v[98:99], v[100:101]
	v_pk_fma_f32 v[94:95], v[94:95], v[146:147], v[144:145] op_sel:[1,0,0] op_sel_hi:[0,1,1]
	v_pk_mul_f32 v[136:137], v[96:97], v[104:105] op_sel:[1,0] op_sel_hi:[0,1]
	v_pk_add_f32 v[94:95], v[94:95], v[98:99]
	v_pk_fma_f32 v[96:97], v[96:97], v[104:105], v[150:151] op_sel:[1,0,0] op_sel_hi:[0,1,1]
	v_pk_add_f32 v[98:99], v[96:97], v[94:95]
	v_cvt_pk_bf16_f32 v94, v120, v140
	v_cvt_pk_bf16_f32 v95, v142, v134
	v_cvt_pk_bf16_f32 v96, v144, v148
	v_cvt_pk_bf16_f32 v97, v150, v136
	v_pk_add_f32 v[114:115], v[114:115], v[98:99]
	v_cvt_pk_bf16_f32 v98, v141, v121
	v_cvt_pk_bf16_f32 v99, v135, v143
	v_cvt_pk_bf16_f32 v100, v149, v145
	v_cvt_pk_bf16_f32 v101, v137, v151
	v_mfma_f32_16x16x32_bf16 v[50:53], v[172:175], v[180:183], v[50:53]
	v_mfma_f32_16x16x32_bf16 v[30:33], v[172:175], v[94:97], v[30:33]
	v_mfma_f32_16x16x32_bf16 v[10:13], v[172:175], v[98:101], v[10:13]
	v_mfma_f32_16x16x32_bf16 v[54:57], v[168:171], v[176:179], v[54:57]
	v_mfma_f32_16x16x32_bf16 v[38:41], v[168:171], v[180:183], v[38:41]
	v_mfma_f32_16x16x32_bf16 v[18:21], v[168:171], v[94:97], v[18:21]
	v_mfma_f32_16x16x32_bf16 v[2:5], v[168:171], v[98:101], v[2:5]
	v_mfma_f32_16x16x32_bf16 v[62:65], v[160:163], v[176:179], v[62:65]
	v_mfma_f32_16x16x32_bf16 v[46:49], v[160:163], v[180:183], v[46:49]
	v_mfma_f32_16x16x32_bf16 v[26:29], v[160:163], v[94:97], v[26:29]
	v_mfma_f32_16x16x32_bf16 v[14:17], v[160:163], v[98:101], v[14:17]
	v_mfma_f32_16x16x32_bf16 v[58:61], v[164:167], v[176:179], v[58:61]
	v_mfma_f32_16x16x32_bf16 v[42:45], v[164:167], v[180:183], v[42:45]
	v_mfma_f32_16x16x32_bf16 v[22:25], v[164:167], v[94:97], v[22:25]
	v_mfma_f32_16x16x32_bf16 v[6:9], v[164:167], v[98:101], v[6:9]
	global_load_dwordx4 v[172:175], v[188:189], off offset:2240
	global_load_dwordx4 v[168:171], v[190:191], off offset:2240
	global_load_dwordx4 v[176:179], v[196:197], off offset:2240
	global_load_dwordx4 v[180:183], v[198:199], off offset:2240
	global_load_dwordx4 v[160:163], v[192:193], off offset:2240
	global_load_dwordx4 v[164:167], v[194:195], off offset:2240
	global_load_dwordx4 v[224:227], v[200:201], off offset:2240
	global_load_dwordx4 v[228:231], v[202:203], off offset:2240
	s_waitcnt vmcnt(8)
	ds_read_b128 v[98:101], v0 offset:256
	ds_read_b128 v[94:97], v0 offset:272
	v_lshlrev_b32_e32 v102, 16, v86
	v_lshlrev_b32_e32 v136, 16, v87
	v_and_b32_e32 v104, 0xffff0000, v86
	v_and_b32_e32 v103, 0xffff0000, v90
	v_and_b32_e32 v137, 0xffff0000, v91
	s_waitcnt lgkmcnt(1)
	v_pk_mul_f32 v[102:103], v[98:99], v[102:103]
	v_lshlrev_b32_e32 v105, 16, v90
	v_pk_mul_f32 v[136:137], v[100:101], v[136:137]
	v_and_b32_e32 v86, 0xffff0000, v87
	v_lshlrev_b32_e32 v87, 16, v91
	v_lshlrev_b32_e32 v138, 16, v88
	v_and_b32_e32 v139, 0xffff0000, v92
	v_pk_mul_f32 v[134:135], v[98:99], v[104:105] op_sel:[1,0] op_sel_hi:[0,1]
	v_pk_mul_f32 v[90:91], v[100:101], v[86:87] op_sel:[1,0] op_sel_hi:[0,1]
	s_waitcnt lgkmcnt(0)
	v_pk_mul_f32 v[138:139], v[94:95], v[138:139]
	v_and_b32_e32 v140, 0xffff0000, v88
	v_lshlrev_b32_e32 v141, 16, v92
	v_lshlrev_b32_e32 v144, 16, v89
	v_and_b32_e32 v145, 0xffff0000, v93
	v_pk_fma_f32 v[104:105], v[98:99], v[104:105], v[102:103] op_sel:[1,0,0] op_sel_hi:[0,1,1]
	v_pk_fma_f32 v[86:87], v[100:101], v[86:87], v[136:137] op_sel:[1,0,0] op_sel_hi:[0,1,1]
	v_pk_mul_f32 v[144:145], v[96:97], v[144:145]
	v_and_b32_e32 v88, 0xffff0000, v89
	v_lshlrev_b32_e32 v89, 16, v93
	v_pk_add_f32 v[86:87], v[104:105], v[86:87]
	v_pk_fma_f32 v[104:105], v[94:95], v[140:141], v[138:139] op_sel:[1,0,0] op_sel_hi:[0,1,1]
	v_pk_mul_f32 v[92:93], v[96:97], v[88:89] op_sel:[1,0] op_sel_hi:[0,1]
	v_pk_add_f32 v[86:87], v[104:105], v[86:87]
	v_pk_fma_f32 v[88:89], v[96:97], v[88:89], v[144:145] op_sel:[1,0,0] op_sel_hi:[0,1,1]
	v_pk_add_f32 v[104:105], v[88:89], v[86:87]
	v_cvt_pk_bf16_f32 v86, v102, v134
	v_cvt_pk_bf16_f32 v87, v136, v90
	v_cvt_pk_bf16_f32 v90, v135, v103
	v_pk_add_f32 v[116:117], v[116:117], v[104:105]
	v_cvt_pk_bf16_f32 v91, v91, v137
	v_pk_mul_f32 v[142:143], v[94:95], v[140:141] op_sel:[1,0] op_sel_hi:[0,1]
	v_cvt_pk_bf16_f32 v88, v138, v142
	v_cvt_pk_bf16_f32 v89, v144, v92
	v_cvt_pk_bf16_f32 v92, v143, v139
	v_cvt_pk_bf16_f32 v93, v93, v145
	v_mfma_f32_16x16x32_bf16 v[66:69], v[82:85], v[86:89], v[66:69]
	v_lshlrev_b32_e32 v120, 16, v152
	v_lshlrev_b32_e32 v142, 16, v153
	v_and_b32_e32 v121, 0xffff0000, v156
	v_and_b32_e32 v143, 0xffff0000, v157
	v_pk_mul_f32 v[120:121], v[98:99], v[120:121]
	v_and_b32_e32 v138, 0xffff0000, v152
	v_lshlrev_b32_e32 v139, 16, v156
	v_pk_mul_f32 v[142:143], v[100:101], v[142:143]
	v_and_b32_e32 v102, 0xffff0000, v153
	v_lshlrev_b32_e32 v103, 16, v157
	v_lshlrev_b32_e32 v144, 16, v154
	v_and_b32_e32 v145, 0xffff0000, v158
	v_pk_mul_f32 v[140:141], v[98:99], v[138:139] op_sel:[1,0] op_sel_hi:[0,1]
	v_pk_mul_f32 v[134:135], v[100:101], v[102:103] op_sel:[1,0] op_sel_hi:[0,1]
	v_pk_mul_f32 v[144:145], v[94:95], v[144:145]
	v_and_b32_e32 v146, 0xffff0000, v154
	v_lshlrev_b32_e32 v147, 16, v158
	v_lshlrev_b32_e32 v150, 16, v155
	v_and_b32_e32 v151, 0xffff0000, v159
	v_pk_fma_f32 v[98:99], v[98:99], v[138:139], v[120:121] op_sel:[1,0,0] op_sel_hi:[0,1,1]
	v_pk_fma_f32 v[100:101], v[100:101], v[102:103], v[142:143] op_sel:[1,0,0] op_sel_hi:[0,1,1]
	v_pk_mul_f32 v[148:149], v[94:95], v[146:147] op_sel:[1,0] op_sel_hi:[0,1]
	v_pk_mul_f32 v[150:151], v[96:97], v[150:151]
	v_and_b32_e32 v104, 0xffff0000, v155
	v_lshlrev_b32_e32 v105, 16, v159
	v_pk_add_f32 v[98:99], v[98:99], v[100:101]
	v_pk_fma_f32 v[94:95], v[94:95], v[146:147], v[144:145] op_sel:[1,0,0] op_sel_hi:[0,1,1]
	v_pk_mul_f32 v[136:137], v[96:97], v[104:105] op_sel:[1,0] op_sel_hi:[0,1]
	v_pk_add_f32 v[94:95], v[94:95], v[98:99]
	v_pk_fma_f32 v[96:97], v[96:97], v[104:105], v[150:151] op_sel:[1,0,0] op_sel_hi:[0,1,1]
	v_pk_add_f32 v[98:99], v[96:97], v[94:95]
	v_cvt_pk_bf16_f32 v94, v120, v140
	v_cvt_pk_bf16_f32 v95, v142, v134
	v_cvt_pk_bf16_f32 v96, v144, v148
	v_cvt_pk_bf16_f32 v97, v150, v136
	v_pk_add_f32 v[114:115], v[114:115], v[98:99]
	v_cvt_pk_bf16_f32 v98, v141, v121
	v_cvt_pk_bf16_f32 v99, v135, v143
	v_cvt_pk_bf16_f32 v100, v149, v145
	v_cvt_pk_bf16_f32 v101, v137, v151
	v_mfma_f32_16x16x32_bf16 v[50:53], v[82:85], v[90:93], v[50:53]
	v_mfma_f32_16x16x32_bf16 v[30:33], v[82:85], v[94:97], v[30:33]
	v_mfma_f32_16x16x32_bf16 v[10:13], v[82:85], v[98:101], v[10:13]
	v_mfma_f32_16x16x32_bf16 v[54:57], v[78:81], v[86:89], v[54:57]
	v_mfma_f32_16x16x32_bf16 v[38:41], v[78:81], v[90:93], v[38:41]
	v_mfma_f32_16x16x32_bf16 v[18:21], v[78:81], v[94:97], v[18:21]
	v_mfma_f32_16x16x32_bf16 v[2:5], v[78:81], v[98:101], v[2:5]
	v_mfma_f32_16x16x32_bf16 v[62:65], v[70:73], v[86:89], v[62:65]
	v_mfma_f32_16x16x32_bf16 v[46:49], v[70:73], v[90:93], v[46:49]
	v_mfma_f32_16x16x32_bf16 v[26:29], v[70:73], v[94:97], v[26:29]
	v_mfma_f32_16x16x32_bf16 v[14:17], v[70:73], v[98:101], v[14:17]
	v_mfma_f32_16x16x32_bf16 v[58:61], v[74:77], v[86:89], v[58:61]
	v_mfma_f32_16x16x32_bf16 v[42:45], v[74:77], v[90:93], v[42:45]
	v_mfma_f32_16x16x32_bf16 v[22:25], v[74:77], v[94:97], v[22:25]
	v_mfma_f32_16x16x32_bf16 v[6:9], v[74:77], v[98:101], v[6:9]
	s_waitcnt vmcnt(0)
	ds_read_b128 v[98:101], v0 offset:384
	ds_read_b128 v[94:97], v0 offset:400
	v_lshlrev_b32_e32 v102, 16, v176
	v_lshlrev_b32_e32 v136, 16, v177
	v_and_b32_e32 v104, 0xffff0000, v176
	v_and_b32_e32 v103, 0xffff0000, v180
	v_and_b32_e32 v137, 0xffff0000, v181
	s_waitcnt lgkmcnt(1)
	v_pk_mul_f32 v[102:103], v[98:99], v[102:103]
	v_lshlrev_b32_e32 v105, 16, v180
	v_pk_mul_f32 v[136:137], v[100:101], v[136:137]
	v_and_b32_e32 v176, 0xffff0000, v177
	v_lshlrev_b32_e32 v177, 16, v181
	v_lshlrev_b32_e32 v138, 16, v178
	v_and_b32_e32 v139, 0xffff0000, v182
	v_pk_mul_f32 v[134:135], v[98:99], v[104:105] op_sel:[1,0] op_sel_hi:[0,1]
	v_pk_mul_f32 v[180:181], v[100:101], v[176:177] op_sel:[1,0] op_sel_hi:[0,1]
	s_waitcnt lgkmcnt(0)
	v_pk_mul_f32 v[138:139], v[94:95], v[138:139]
	v_and_b32_e32 v140, 0xffff0000, v178
	v_lshlrev_b32_e32 v141, 16, v182
	v_lshlrev_b32_e32 v144, 16, v179
	v_and_b32_e32 v145, 0xffff0000, v183
	v_pk_fma_f32 v[104:105], v[98:99], v[104:105], v[102:103] op_sel:[1,0,0] op_sel_hi:[0,1,1]
	v_pk_fma_f32 v[176:177], v[100:101], v[176:177], v[136:137] op_sel:[1,0,0] op_sel_hi:[0,1,1]
	v_pk_mul_f32 v[144:145], v[96:97], v[144:145]
	v_and_b32_e32 v178, 0xffff0000, v179
	v_lshlrev_b32_e32 v179, 16, v183
	v_pk_add_f32 v[176:177], v[104:105], v[176:177]
	v_pk_fma_f32 v[104:105], v[94:95], v[140:141], v[138:139] op_sel:[1,0,0] op_sel_hi:[0,1,1]
	v_pk_mul_f32 v[182:183], v[96:97], v[178:179] op_sel:[1,0] op_sel_hi:[0,1]
	v_pk_add_f32 v[176:177], v[104:105], v[176:177]
	v_pk_fma_f32 v[178:179], v[96:97], v[178:179], v[144:145] op_sel:[1,0,0] op_sel_hi:[0,1,1]
	v_pk_add_f32 v[104:105], v[178:179], v[176:177]
	v_cvt_pk_bf16_f32 v176, v102, v134
	v_cvt_pk_bf16_f32 v177, v136, v180
	v_cvt_pk_bf16_f32 v180, v135, v103
	v_pk_add_f32 v[116:117], v[116:117], v[104:105]
	v_cvt_pk_bf16_f32 v181, v181, v137
	v_pk_mul_f32 v[142:143], v[94:95], v[140:141] op_sel:[1,0] op_sel_hi:[0,1]
	v_cvt_pk_bf16_f32 v178, v138, v142
	v_cvt_pk_bf16_f32 v179, v144, v182
	v_cvt_pk_bf16_f32 v182, v143, v139
	v_cvt_pk_bf16_f32 v183, v183, v145
	v_mfma_f32_16x16x32_bf16 v[66:69], v[172:175], v[176:179], v[66:69]
	v_lshlrev_b32_e32 v120, 16, v224
	v_lshlrev_b32_e32 v142, 16, v225
	v_and_b32_e32 v121, 0xffff0000, v228
	v_and_b32_e32 v143, 0xffff0000, v229
	v_pk_mul_f32 v[120:121], v[98:99], v[120:121]
	v_and_b32_e32 v138, 0xffff0000, v224
	v_lshlrev_b32_e32 v139, 16, v228
	v_pk_mul_f32 v[142:143], v[100:101], v[142:143]
	v_and_b32_e32 v102, 0xffff0000, v225
	v_lshlrev_b32_e32 v103, 16, v229
	v_lshlrev_b32_e32 v144, 16, v226
	v_and_b32_e32 v145, 0xffff0000, v230
	v_pk_mul_f32 v[140:141], v[98:99], v[138:139] op_sel:[1,0] op_sel_hi:[0,1]
	v_pk_mul_f32 v[134:135], v[100:101], v[102:103] op_sel:[1,0] op_sel_hi:[0,1]
	v_pk_mul_f32 v[144:145], v[94:95], v[144:145]
	v_and_b32_e32 v146, 0xffff0000, v226
	v_lshlrev_b32_e32 v147, 16, v230
	v_lshlrev_b32_e32 v150, 16, v227
	v_and_b32_e32 v151, 0xffff0000, v231
	v_pk_fma_f32 v[98:99], v[98:99], v[138:139], v[120:121] op_sel:[1,0,0] op_sel_hi:[0,1,1]
	v_pk_fma_f32 v[100:101], v[100:101], v[102:103], v[142:143] op_sel:[1,0,0] op_sel_hi:[0,1,1]
	v_pk_mul_f32 v[148:149], v[94:95], v[146:147] op_sel:[1,0] op_sel_hi:[0,1]
	v_pk_mul_f32 v[150:151], v[96:97], v[150:151]
	v_and_b32_e32 v104, 0xffff0000, v227
	v_lshlrev_b32_e32 v105, 16, v231
	v_pk_add_f32 v[98:99], v[98:99], v[100:101]
	v_pk_fma_f32 v[94:95], v[94:95], v[146:147], v[144:145] op_sel:[1,0,0] op_sel_hi:[0,1,1]
	v_pk_mul_f32 v[136:137], v[96:97], v[104:105] op_sel:[1,0] op_sel_hi:[0,1]
	v_pk_add_f32 v[94:95], v[94:95], v[98:99]
	v_pk_fma_f32 v[96:97], v[96:97], v[104:105], v[150:151] op_sel:[1,0,0] op_sel_hi:[0,1,1]
	v_pk_add_f32 v[98:99], v[96:97], v[94:95]
	v_cvt_pk_bf16_f32 v94, v120, v140
	v_cvt_pk_bf16_f32 v95, v142, v134
	v_cvt_pk_bf16_f32 v96, v144, v148
	v_cvt_pk_bf16_f32 v97, v150, v136
	v_pk_add_f32 v[114:115], v[114:115], v[98:99]
	v_cvt_pk_bf16_f32 v98, v141, v121
	v_cvt_pk_bf16_f32 v99, v135, v143
	v_cvt_pk_bf16_f32 v100, v149, v145
	v_cvt_pk_bf16_f32 v101, v137, v151
	v_mfma_f32_16x16x32_bf16 v[50:53], v[172:175], v[180:183], v[50:53]
	v_mfma_f32_16x16x32_bf16 v[30:33], v[172:175], v[94:97], v[30:33]
	v_mfma_f32_16x16x32_bf16 v[10:13], v[172:175], v[98:101], v[10:13]
	v_mfma_f32_16x16x32_bf16 v[54:57], v[168:171], v[176:179], v[54:57]
	v_mfma_f32_16x16x32_bf16 v[38:41], v[168:171], v[180:183], v[38:41]
	v_mfma_f32_16x16x32_bf16 v[18:21], v[168:171], v[94:97], v[18:21]
	v_mfma_f32_16x16x32_bf16 v[2:5], v[168:171], v[98:101], v[2:5]
	v_mfma_f32_16x16x32_bf16 v[62:65], v[160:163], v[176:179], v[62:65]
	v_mfma_f32_16x16x32_bf16 v[46:49], v[160:163], v[180:183], v[46:49]
	v_mfma_f32_16x16x32_bf16 v[26:29], v[160:163], v[94:97], v[26:29]
	v_mfma_f32_16x16x32_bf16 v[14:17], v[160:163], v[98:101], v[14:17]
	v_mfma_f32_16x16x32_bf16 v[58:61], v[164:167], v[176:179], v[58:61]
	v_mfma_f32_16x16x32_bf16 v[42:45], v[164:167], v[180:183], v[42:45]
	v_mfma_f32_16x16x32_bf16 v[22:25], v[164:167], v[94:97], v[22:25]
	v_mfma_f32_16x16x32_bf16 v[6:9], v[164:167], v[98:101], v[6:9]
	v_lshlrev_b64 v[72:73], 14, v[106:107]
	ds_bpermute_b32 v0, v127, v116
	v_lshl_add_u64 v[72:73], v[110:111], 0, v[72:73]
	global_store_dword v[72:73], v66, off
	global_store_dword v[72:73], v67, off offset:256
	global_store_dword v[72:73], v68, off offset:512
	global_store_dword v[72:73], v69, off offset:768
	v_add_co_u32_e32 v66, vcc, 0x1000, v72
	s_movk_i32 s30, 0x2000
	s_nop 0
	v_addc_co_u32_e32 v67, vcc, 0, v73, vcc
	global_store_dword v[66:67], v54, off
	global_store_dword v[66:67], v55, off offset:256
	global_store_dword v[66:67], v56, off offset:512
	global_store_dword v[66:67], v57, off offset:768
	v_add_co_u32_e32 v54, vcc, s30, v72
	s_waitcnt lgkmcnt(0)
	v_add_f32_e32 v0, v116, v0
	v_addc_co_u32_e32 v55, vcc, 0, v73, vcc
	global_store_dword v[54:55], v62, off
	global_store_dword v[54:55], v63, off offset:256
	global_store_dword v[54:55], v64, off offset:512
	global_store_dword v[54:55], v65, off offset:768
	ds_bpermute_b32 v54, v128, v0
	v_lshlrev_b64 v[70:71], 8, v[106:107]
	v_add_co_u32_e32 v56, vcc, 0x3000, v72
	v_lshl_add_u64 v[70:71], v[108:109], 0, v[70:71]
	s_nop 0
	v_addc_co_u32_e32 v57, vcc, 0, v73, vcc
	global_store_dword v[56:57], v58, off
	global_store_dword v[56:57], v59, off offset:256
	global_store_dword v[56:57], v60, off offset:512
	global_store_dword v[56:57], v61, off offset:768
	s_and_saveexec_b64 s[30:31], s[2:3]
	s_cbranch_execz .LBB0_663
	s_waitcnt lgkmcnt(0)
	v_add_f32_e32 v0, v0, v54
	global_store_dword v[70:71], v0, off
